# v75 + P3 ticket queue split into 8192 single jobs (even: dilated-attention unit, odd: its 12 conversion items) instead of 4096 unit+items pairs
# baseline (speedup 1.0000x reference)
.LBB0_328:
	s_or_b64 exec, exec, s[0:1]
	v_readfirstlane_b32 s22, v0
	s_cmpk_gt_u32 s22, 0x1fff
	s_mov_b64 s[0:1], -1
	s_cbranch_scc1 .LBB0_323
	s_and_b32 s91, s22, 1
	s_lshr_b32 s22, s22, 1
	s_cmp_eq_u32 s91, 0
	s_cbranch_scc1 .Ldil_start
	s_mul_i32 s20, s22, 12
	s_mov_b32 s23, 0
	s_branch .Lcv3_entry
